# router: the eight logit wave-sums reduced hop-by-hop together (6 LDS round trips per token instead of ~45)
# speedup vs baseline: 1.0046x; 1.0046x over previous
.LBB0_1622:
	v_lshl_add_u64 v[0:1], s[52:53], 0, v[18:19]
	s_waitcnt lgkmcnt(0)
	v_add_co_u32_e32 v20, vcc, 0x2d000000, v0
	s_nop 1
	v_addc_co_u32_e32 v21, vcc, 0, v1, vcc
	global_load_dwordx2 v[60:61], v[20:21], off
	global_load_dwordx2 v[62:63], v[20:21], off offset:512
	global_load_dwordx2 v[64:65], v[20:21], off offset:1024
	global_load_dwordx2 v[66:67], v[20:21], off offset:1536
	global_load_dwordx2 v[68:69], v[20:21], off offset:2048
	global_load_dwordx2 v[70:71], v[20:21], off offset:2560
	global_load_dwordx2 v[72:73], v[20:21], off offset:3072
	global_load_dwordx2 v[74:75], v[20:21], off offset:3584
	s_waitcnt vmcnt(7)
	v_mov_b32_e32 v0, v60
	v_mov_b32_e32 v1, v61
	v_lshlrev_b32_e32 v26, 16, v0
	v_and_b32_e32 v28, 0xffff0000, v0
	v_lshlrev_b32_e32 v30, 16, v1
	v_and_b32_e32 v32, 0xffff0000, v1
	ds_read_b128 v[0:3], v25
	ds_read_b128 v[4:7], v25 offset:32768
	v_mul_f32_e32 v40, v28, v28
	v_fmac_f32_e32 v40, v26, v26
	v_fmac_f32_e32 v40, v30, v30
	s_waitcnt lgkmcnt(1)
	v_fma_f32 v39, v2, v26, 0
	v_fma_f32 v37, v3, v26, 0
	s_waitcnt lgkmcnt(0)
	v_fma_f32 v35, v4, v26, 0
	v_fma_f32 v33, v5, v26, 0
	v_fma_f32 v31, v6, v26, 0
	v_fma_f32 v29, v7, v26, 0
	ds_read_b128 v[2:5], v25 offset:8192
	ds_read_b128 v[6:9], v25 offset:40960
	v_pk_fma_f32 v[0:1], v[0:1], v[26:27], 0 op_sel_hi:[1,0,0]
	v_fmac_f32_e32 v40, v32, v32
	s_waitcnt lgkmcnt(1)
	v_fmac_f32_e32 v39, v4, v28
	v_fmac_f32_e32 v37, v5, v28
	s_waitcnt lgkmcnt(0)
	v_fmac_f32_e32 v35, v6, v28
	v_fmac_f32_e32 v33, v7, v28
	v_fmac_f32_e32 v31, v8, v28
	v_fmac_f32_e32 v29, v9, v28
	ds_read_b128 v[4:7], v25 offset:16384
	ds_read_b128 v[8:11], v25 offset:49152
	s_waitcnt lgkmcnt(1)
	v_fmac_f32_e32 v39, v6, v30
	v_fmac_f32_e32 v37, v7, v30
	s_waitcnt lgkmcnt(0)
	v_fmac_f32_e32 v35, v8, v30
	v_fmac_f32_e32 v33, v9, v30
	v_fmac_f32_e32 v31, v10, v30
	v_fmac_f32_e32 v29, v11, v30
	ds_read_b128 v[6:9], v25 offset:24576
	ds_read_b128 v[10:13], v25 offset:57344
	s_waitcnt lgkmcnt(1)
	v_fmac_f32_e32 v39, v8, v32
	v_fmac_f32_e32 v37, v9, v32
	s_waitcnt lgkmcnt(0)
	v_fmac_f32_e32 v35, v10, v32
	v_fmac_f32_e32 v33, v11, v32
	v_fmac_f32_e32 v31, v12, v32
	v_fmac_f32_e32 v29, v13, v32
	v_pk_fma_f32 v[0:1], v[2:3], v[28:29], v[0:1] op_sel_hi:[1,0,1]
	s_waitcnt vmcnt(6)
	v_mov_b32_e32 v8, v62
	v_mov_b32_e32 v9, v63
	v_lshlrev_b32_e32 v34, 16, v8
	v_and_b32_e32 v16, 0xffff0000, v8
	v_lshlrev_b32_e32 v22, 16, v9
	v_and_b32_e32 v24, 0xffff0000, v9
	ds_read_b128 v[8:11], v25 offset:1024
	ds_read_b128 v[12:15], v25 offset:33792
	v_pk_fma_f32 v[0:1], v[4:5], v[30:31], v[0:1] op_sel_hi:[1,0,1]
	v_fmac_f32_e32 v40, v34, v34
	v_pk_fma_f32 v[0:1], v[6:7], v[32:33], v[0:1] op_sel_hi:[1,0,1]
	s_waitcnt lgkmcnt(1)
	v_fmac_f32_e32 v39, v10, v34
	v_pk_fma_f32 v[26:27], v[8:9], v[34:35], v[0:1] op_sel_hi:[1,0,1]
	ds_read_b128 v[0:3], v25 offset:9216
	ds_read_b128 v[4:7], v25 offset:41984
	v_fmac_f32_e32 v37, v11, v34
	s_waitcnt lgkmcnt(2)
	v_fmac_f32_e32 v35, v12, v34
	v_fmac_f32_e32 v33, v13, v34
	v_fmac_f32_e32 v31, v14, v34
	v_fmac_f32_e32 v29, v15, v34
	s_waitcnt lgkmcnt(1)
	v_fmac_f32_e32 v39, v2, v16
	v_fmac_f32_e32 v37, v3, v16
	s_waitcnt lgkmcnt(0)
	v_fmac_f32_e32 v35, v4, v16
	v_fmac_f32_e32 v33, v5, v16
	v_fmac_f32_e32 v31, v6, v16
	v_fmac_f32_e32 v29, v7, v16
	ds_read_b128 v[2:5], v25 offset:17408
	ds_read_b128 v[6:9], v25 offset:50176
	v_pk_fma_f32 v[0:1], v[0:1], v[16:17], v[26:27] op_sel_hi:[1,0,1]
	v_fmac_f32_e32 v40, v16, v16
	v_fmac_f32_e32 v40, v22, v22
	s_waitcnt lgkmcnt(1)
	v_fmac_f32_e32 v39, v4, v22
	v_fmac_f32_e32 v37, v5, v22
	s_waitcnt lgkmcnt(0)
	v_fmac_f32_e32 v35, v6, v22
	v_fmac_f32_e32 v33, v7, v22
	v_fmac_f32_e32 v31, v8, v22
	v_fmac_f32_e32 v29, v9, v22
	ds_read_b128 v[4:7], v25 offset:25600
	ds_read_b128 v[8:11], v25 offset:58368
	v_pk_fma_f32 v[0:1], v[2:3], v[22:23], v[0:1] op_sel_hi:[1,0,1]
	v_fmac_f32_e32 v40, v24, v24
	s_waitcnt lgkmcnt(1)
	v_fmac_f32_e32 v39, v6, v24
	v_fmac_f32_e32 v37, v7, v24
	s_waitcnt lgkmcnt(0)
	v_fmac_f32_e32 v35, v8, v24
	v_fmac_f32_e32 v33, v9, v24
	v_fmac_f32_e32 v31, v10, v24
	v_fmac_f32_e32 v29, v11, v24
	v_pk_fma_f32 v[0:1], v[4:5], v[24:25], v[0:1] op_sel_hi:[1,0,1]
	s_waitcnt vmcnt(5)
	v_mov_b32_e32 v6, v64
	v_mov_b32_e32 v7, v65
	v_lshlrev_b32_e32 v28, 16, v6
	v_and_b32_e32 v30, 0xffff0000, v6
	v_lshlrev_b32_e32 v32, 16, v7
	v_and_b32_e32 v34, 0xffff0000, v7
	ds_read_b128 v[6:9], v25 offset:2048
	ds_read_b128 v[10:13], v25 offset:34816
	v_fmac_f32_e32 v40, v28, v28
	v_fmac_f32_e32 v40, v30, v30
	v_fmac_f32_e32 v40, v32, v32
	s_waitcnt lgkmcnt(1)
	v_fmac_f32_e32 v39, v8, v28
	v_fmac_f32_e32 v37, v9, v28
	s_waitcnt lgkmcnt(0)
	v_fmac_f32_e32 v35, v10, v28
	v_fmac_f32_e32 v33, v11, v28
	v_fmac_f32_e32 v31, v12, v28
	v_fmac_f32_e32 v29, v13, v28
	ds_read_b128 v[8:11], v25 offset:10240
	ds_read_b128 v[12:15], v25 offset:43008
	v_fmac_f32_e32 v40, v34, v34
	s_waitcnt lgkmcnt(1)
	v_fmac_f32_e32 v39, v10, v30
	v_fmac_f32_e32 v37, v11, v30
	s_waitcnt lgkmcnt(0)
	v_fmac_f32_e32 v35, v12, v30
	v_fmac_f32_e32 v33, v13, v30
	ds_read_b128 v[10:13], v25 offset:18432
	ds_read_b128 v[42:45], v25 offset:51200
	v_fmac_f32_e32 v31, v14, v30
	v_fmac_f32_e32 v29, v15, v30
	s_waitcnt lgkmcnt(1)
	v_fmac_f32_e32 v39, v12, v32
	v_fmac_f32_e32 v37, v13, v32
	s_waitcnt lgkmcnt(0)
	v_fmac_f32_e32 v35, v42, v32
	v_fmac_f32_e32 v33, v43, v32
	v_fmac_f32_e32 v31, v44, v32
	v_fmac_f32_e32 v29, v45, v32
	ds_read_b128 v[12:15], v25 offset:26624
	ds_read_b128 v[42:45], v25 offset:59392
	s_waitcnt lgkmcnt(1)
	v_fmac_f32_e32 v39, v14, v34
	v_fmac_f32_e32 v37, v15, v34
	s_waitcnt lgkmcnt(0)
	v_fmac_f32_e32 v35, v42, v34
	v_fmac_f32_e32 v33, v43, v34
	v_fmac_f32_e32 v31, v44, v34
	v_fmac_f32_e32 v29, v45, v34
	ds_read_b128 v[42:45], v25 offset:3072
	ds_read_b128 v[46:49], v25 offset:35840
	s_waitcnt vmcnt(4)
	v_mov_b32_e32 v14, v66
	v_mov_b32_e32 v15, v67
	v_lshlrev_b32_e32 v36, 16, v14
	s_waitcnt lgkmcnt(1)
	v_fmac_f32_e32 v39, v44, v36
	v_fmac_f32_e32 v37, v45, v36
	s_waitcnt lgkmcnt(0)
	v_fmac_f32_e32 v35, v46, v36
	v_fmac_f32_e32 v33, v47, v36
	v_fmac_f32_e32 v31, v48, v36
	v_fmac_f32_e32 v29, v49, v36
	ds_read_b128 v[44:47], v25 offset:11264
	ds_read_b128 v[48:51], v25 offset:44032
	v_and_b32_e32 v14, 0xffff0000, v14
	v_lshlrev_b32_e32 v38, 16, v15
	v_and_b32_e32 v56, 0xffff0000, v15
	s_waitcnt lgkmcnt(1)
	v_fmac_f32_e32 v39, v46, v14
	v_fmac_f32_e32 v37, v47, v14
	s_waitcnt lgkmcnt(0)
	v_fmac_f32_e32 v35, v48, v14
	v_fmac_f32_e32 v33, v49, v14
	v_fmac_f32_e32 v31, v50, v14
	v_fmac_f32_e32 v29, v51, v14
	ds_read_b128 v[46:49], v25 offset:19456
	ds_read_b128 v[50:53], v25 offset:52224
	v_fmac_f32_e32 v40, v36, v36
	v_fmac_f32_e32 v40, v14, v14
	v_fmac_f32_e32 v40, v38, v38
	s_waitcnt lgkmcnt(1)
	v_fmac_f32_e32 v39, v48, v38
	s_waitcnt lgkmcnt(0)
	v_fmac_f32_e32 v29, v53, v38
	v_fmac_f32_e32 v31, v52, v38
	v_pk_fma_f32 v[0:1], v[6:7], v[28:29], v[0:1] op_sel_hi:[1,0,1]
	v_fmac_f32_e32 v33, v51, v38
	v_pk_fma_f32 v[0:1], v[8:9], v[30:31], v[0:1] op_sel_hi:[1,0,1]
	v_fmac_f32_e32 v35, v50, v38
	v_pk_fma_f32 v[0:1], v[10:11], v[32:33], v[0:1] op_sel_hi:[1,0,1]
	v_fmac_f32_e32 v37, v49, v38
	ds_read_b128 v[48:51], v25 offset:27648
	ds_read_b128 v[52:55], v25 offset:60416
	v_pk_fma_f32 v[0:1], v[12:13], v[34:35], v[0:1] op_sel_hi:[1,0,1]
	v_fmac_f32_e32 v40, v56, v56
	v_pk_fma_f32 v[0:1], v[42:43], v[36:37], v[0:1] op_sel_hi:[1,0,1]
	s_waitcnt lgkmcnt(1)
	v_fmac_f32_e32 v37, v51, v56
	v_pk_fma_f32 v[0:1], v[44:45], v[14:15], v[0:1] op_sel_hi:[1,0,1]
	s_waitcnt lgkmcnt(0)
	v_fmac_f32_e32 v35, v52, v56
	v_pk_fma_f32 v[0:1], v[46:47], v[38:39], v[0:1] op_sel_hi:[1,0,1]
	v_fmac_f32_e32 v39, v50, v56
	v_pk_fma_f32 v[22:23], v[48:49], v[56:57], v[0:1] op_sel_hi:[1,0,1]
	v_fmac_f32_e32 v33, v53, v56
	v_fmac_f32_e32 v31, v54, v56
	v_fmac_f32_e32 v29, v55, v56
	s_waitcnt vmcnt(3)
	v_mov_b32_e32 v0, v68
	v_mov_b32_e32 v1, v69
	v_lshlrev_b32_e32 v24, 16, v0
	v_and_b32_e32 v26, 0xffff0000, v0
	v_lshlrev_b32_e32 v28, 16, v1
	v_and_b32_e32 v30, 0xffff0000, v1
	ds_read_b128 v[0:3], v25 offset:4096
	ds_read_b128 v[4:7], v25 offset:36864
	v_fmac_f32_e32 v40, v24, v24
	v_fmac_f32_e32 v40, v26, v26
	v_fmac_f32_e32 v40, v28, v28
	s_waitcnt lgkmcnt(1)
	v_fmac_f32_e32 v39, v2, v24
	v_fmac_f32_e32 v37, v3, v24
	s_waitcnt lgkmcnt(0)
	v_fmac_f32_e32 v35, v4, v24
	v_fmac_f32_e32 v33, v5, v24
	v_fmac_f32_e32 v31, v6, v24
	v_fmac_f32_e32 v29, v7, v24
	ds_read_b128 v[2:5], v25 offset:12288
	ds_read_b128 v[6:9], v25 offset:45056
	v_pk_fma_f32 v[0:1], v[0:1], v[24:25], v[22:23] op_sel_hi:[1,0,1]
	v_fmac_f32_e32 v40, v30, v30
	s_waitcnt lgkmcnt(1)
	v_fmac_f32_e32 v39, v4, v26
	v_fmac_f32_e32 v37, v5, v26
	s_waitcnt lgkmcnt(0)
	v_fmac_f32_e32 v35, v6, v26
	v_fmac_f32_e32 v33, v7, v26
	v_fmac_f32_e32 v31, v8, v26
	v_fmac_f32_e32 v29, v9, v26
	ds_read_b128 v[4:7], v25 offset:20480
	ds_read_b128 v[8:11], v25 offset:53248
	v_pk_fma_f32 v[0:1], v[2:3], v[26:27], v[0:1] op_sel_hi:[1,0,1]
	s_waitcnt lgkmcnt(1)
	v_fmac_f32_e32 v39, v6, v28
	v_fmac_f32_e32 v37, v7, v28
	s_waitcnt lgkmcnt(0)
	v_fmac_f32_e32 v35, v8, v28
	v_fmac_f32_e32 v33, v9, v28
	v_fmac_f32_e32 v31, v10, v28
	v_fmac_f32_e32 v29, v11, v28
	ds_read_b128 v[6:9], v25 offset:28672
	ds_read_b128 v[10:13], v25 offset:61440
	s_waitcnt lgkmcnt(1)
	v_fmac_f32_e32 v39, v8, v30
	v_fmac_f32_e32 v37, v9, v30
	s_waitcnt lgkmcnt(0)
	v_fmac_f32_e32 v35, v10, v30
	v_fmac_f32_e32 v33, v11, v30
	v_fmac_f32_e32 v31, v12, v30
	v_fmac_f32_e32 v29, v13, v30
	s_waitcnt vmcnt(2)
	v_mov_b32_e32 v8, v70
	v_mov_b32_e32 v9, v71
	v_lshlrev_b32_e32 v32, 16, v8
	v_and_b32_e32 v34, 0xffff0000, v8
	v_lshlrev_b32_e32 v36, 16, v9
	v_and_b32_e32 v38, 0xffff0000, v9
	ds_read_b128 v[8:11], v25 offset:5120
	ds_read_b128 v[12:15], v25 offset:37888
	v_fmac_f32_e32 v40, v32, v32
	v_fmac_f32_e32 v40, v34, v34
	v_fmac_f32_e32 v40, v36, v36
	s_waitcnt lgkmcnt(1)
	v_fmac_f32_e32 v39, v10, v32
	v_fmac_f32_e32 v37, v11, v32
	s_waitcnt lgkmcnt(0)
	v_fmac_f32_e32 v35, v12, v32
	v_fmac_f32_e32 v33, v13, v32
	v_fmac_f32_e32 v31, v14, v32
	v_fmac_f32_e32 v29, v15, v32
	ds_read_b128 v[10:13], v25 offset:13312
	ds_read_b128 v[14:17], v25 offset:46080
	v_fmac_f32_e32 v40, v38, v38
	s_waitcnt lgkmcnt(1)
	v_fmac_f32_e32 v39, v12, v34
	v_fmac_f32_e32 v37, v13, v34
	s_waitcnt lgkmcnt(0)
	v_fmac_f32_e32 v35, v14, v34
	v_fmac_f32_e32 v33, v15, v34
	ds_read_b128 v[12:15], v25 offset:21504
	ds_read_b128 v[42:45], v25 offset:54272
	v_fmac_f32_e32 v31, v16, v34
	v_fmac_f32_e32 v29, v17, v34
	s_waitcnt lgkmcnt(1)
	v_fmac_f32_e32 v39, v14, v36
	v_fmac_f32_e32 v37, v15, v36
	s_waitcnt lgkmcnt(0)
	v_fmac_f32_e32 v35, v42, v36
	v_fmac_f32_e32 v33, v43, v36
	v_fmac_f32_e32 v31, v44, v36
	v_fmac_f32_e32 v29, v45, v36
	ds_read_b128 v[14:17], v25 offset:29696
	ds_read_b128 v[42:45], v25 offset:62464
	s_waitcnt lgkmcnt(1)
	v_fmac_f32_e32 v39, v16, v38
	v_fmac_f32_e32 v37, v17, v38
	s_waitcnt lgkmcnt(0)
	v_fmac_f32_e32 v35, v42, v38
	v_fmac_f32_e32 v33, v43, v38
	v_fmac_f32_e32 v31, v44, v38
	v_fmac_f32_e32 v29, v45, v38
	ds_read_b128 v[42:45], v25 offset:6144
	ds_read_b128 v[46:49], v25 offset:38912
	s_waitcnt vmcnt(1)
	v_mov_b32_e32 v16, v72
	v_mov_b32_e32 v17, v73
	v_lshlrev_b32_e32 v54, 16, v16
	s_waitcnt lgkmcnt(1)
	v_fmac_f32_e32 v39, v44, v54
	v_fmac_f32_e32 v37, v45, v54
	s_waitcnt lgkmcnt(0)
	v_fmac_f32_e32 v35, v46, v54
	v_fmac_f32_e32 v33, v47, v54
	v_fmac_f32_e32 v31, v48, v54
	v_fmac_f32_e32 v29, v49, v54
	ds_read_b128 v[44:47], v25 offset:14336
	ds_read_b128 v[48:51], v25 offset:47104
	v_and_b32_e32 v56, 0xffff0000, v16
	v_lshlrev_b32_e32 v58, 16, v17
	v_and_b32_e32 v16, 0xffff0000, v17
	s_waitcnt lgkmcnt(1)
	v_fmac_f32_e32 v37, v47, v56
	s_waitcnt lgkmcnt(0)
	v_fmac_f32_e32 v29, v51, v56
	v_fmac_f32_e32 v31, v50, v56
	v_pk_fma_f32 v[0:1], v[4:5], v[28:29], v[0:1] op_sel_hi:[1,0,1]
	v_fmac_f32_e32 v33, v49, v56
	v_pk_fma_f32 v[0:1], v[6:7], v[30:31], v[0:1] op_sel_hi:[1,0,1]
	v_fmac_f32_e32 v35, v48, v56
	v_pk_fma_f32 v[0:1], v[8:9], v[32:33], v[0:1] op_sel_hi:[1,0,1]
	v_fmac_f32_e32 v39, v46, v56
	v_pk_fma_f32 v[0:1], v[10:11], v[34:35], v[0:1] op_sel_hi:[1,0,1]
	ds_read_b128 v[46:49], v25 offset:22528
	ds_read_b128 v[50:53], v25 offset:55296
	v_pk_fma_f32 v[0:1], v[12:13], v[36:37], v[0:1] op_sel_hi:[1,0,1]
	v_fmac_f32_e32 v40, v54, v54
	v_pk_fma_f32 v[0:1], v[14:15], v[38:39], v[0:1] op_sel_hi:[1,0,1]
	s_waitcnt lgkmcnt(1)
	v_fmac_f32_e32 v39, v48, v58
	v_pk_fma_f32 v[0:1], v[42:43], v[54:55], v[0:1] op_sel_hi:[1,0,1]
	v_fmac_f32_e32 v37, v49, v58
	v_pk_fma_f32 v[0:1], v[44:45], v[56:57], v[0:1] op_sel_hi:[1,0,1]
	s_waitcnt lgkmcnt(0)
	v_fmac_f32_e32 v35, v50, v58
	v_pk_fma_f32 v[12:13], v[46:47], v[58:59], v[0:1] op_sel_hi:[1,0,1]
	ds_read_b128 v[0:3], v25 offset:30720
	ds_read_b128 v[4:7], v25 offset:63488
	v_fmac_f32_e32 v33, v51, v58
	v_fmac_f32_e32 v31, v52, v58
	v_fmac_f32_e32 v29, v53, v58
	s_waitcnt lgkmcnt(1)
	v_fmac_f32_e32 v39, v2, v16
	v_fmac_f32_e32 v37, v3, v16
	s_waitcnt lgkmcnt(0)
	v_fmac_f32_e32 v35, v4, v16
	v_fmac_f32_e32 v33, v5, v16
	v_fmac_f32_e32 v31, v6, v16
	v_fmac_f32_e32 v29, v7, v16
	v_fmac_f32_e32 v40, v56, v56
	v_fmac_f32_e32 v40, v58, v58
	v_fmac_f32_e32 v40, v16, v16
	s_waitcnt vmcnt(0)
	v_mov_b32_e32 v2, v74
	v_mov_b32_e32 v3, v75
	v_lshlrev_b32_e32 v24, 16, v2
	v_and_b32_e32 v22, 0xffff0000, v2
	v_lshlrev_b32_e32 v20, 16, v3
	v_and_b32_e32 v14, 0xffff0000, v3
	ds_read_b128 v[2:5], v25 offset:7168
	ds_read_b128 v[6:9], v25 offset:39936
	v_fmac_f32_e32 v40, v24, v24
	v_fmac_f32_e32 v40, v22, v22
	v_fmac_f32_e32 v40, v20, v20
	s_waitcnt lgkmcnt(1)
	v_fmac_f32_e32 v39, v4, v24
	v_fmac_f32_e32 v37, v5, v24
	s_waitcnt lgkmcnt(0)
	v_fmac_f32_e32 v35, v6, v24
	v_fmac_f32_e32 v33, v7, v24
	v_fmac_f32_e32 v31, v8, v24
	v_fmac_f32_e32 v29, v9, v24
	ds_read_b128 v[4:7], v25 offset:15360
	ds_read_b128 v[8:11], v25 offset:48128
	v_fmac_f32_e32 v40, v14, v14
	s_waitcnt lgkmcnt(1)
	v_fmac_f32_e32 v39, v6, v22
	v_fmac_f32_e32 v37, v7, v22
	s_waitcnt lgkmcnt(0)
	v_fmac_f32_e32 v35, v8, v22
	v_fmac_f32_e32 v33, v9, v22
	ds_read_b128 v[6:9], v25 offset:23552
	ds_read_b128 v[42:45], v25 offset:56320
	v_fmac_f32_e32 v31, v10, v22
	v_fmac_f32_e32 v29, v11, v22
	s_waitcnt lgkmcnt(1)
	v_fmac_f32_e32 v39, v8, v20
	v_fmac_f32_e32 v37, v9, v20
	s_waitcnt lgkmcnt(0)
	v_fmac_f32_e32 v35, v42, v20
	v_fmac_f32_e32 v33, v43, v20
	v_fmac_f32_e32 v31, v44, v20
	v_fmac_f32_e32 v29, v45, v20
	ds_read_b128 v[8:11], v25 offset:31744
	ds_read_b128 v[42:45], v25 offset:64512
	s_waitcnt lgkmcnt(1)
	v_fmac_f32_e32 v39, v10, v14
	v_mbcnt_lo_u32_b32 v10, -1, 0
	v_mbcnt_hi_u32_b32 v10, -1, v10
	v_fmac_f32_e32 v37, v11, v14
	v_lshlrev_b32_e32 v10, 2, v10
	v_xor_b32_e32 v10, 4, v10
	ds_bpermute_b32 v10, v10, v40
	v_mbcnt_lo_u32_b32 v11, -1, 0
	v_mbcnt_hi_u32_b32 v11, -1, v11
	s_waitcnt lgkmcnt(1)
	v_fmac_f32_e32 v35, v42, v14
	v_lshlrev_b32_e32 v11, 2, v11
	v_xor_b32_e32 v11, 8, v11
	s_waitcnt lgkmcnt(0)
	v_add_f32_e32 v10, v40, v10
	ds_bpermute_b32 v11, v11, v10
	v_fmac_f32_e32 v33, v43, v14
	v_fmac_f32_e32 v31, v44, v14
	v_fmac_f32_e32 v29, v45, v14
	s_waitcnt lgkmcnt(0)
	v_add_f32_e32 v10, v10, v11
	v_mbcnt_lo_u32_b32 v11, -1, 0
	v_mbcnt_hi_u32_b32 v11, -1, v11
	s_nop 0
	v_lshlrev_b32_e32 v11, 2, v11
	v_xor_b32_e32 v11, 16, v11
	ds_bpermute_b32 v11, v11, v10
	s_waitcnt lgkmcnt(0)
	v_add_f32_e32 v10, v10, v11
	v_mbcnt_lo_u32_b32 v11, -1, 0
	v_mbcnt_hi_u32_b32 v11, -1, v11
	s_nop 0
	v_lshlrev_b32_e32 v11, 2, v11
	v_xor_b32_e32 v11, 32, v11
	ds_bpermute_b32 v11, v11, v10
	s_waitcnt lgkmcnt(0)
	v_add_f32_e32 v10, v10, v11
	v_mbcnt_lo_u32_b32 v11, -1, 0
	v_mbcnt_hi_u32_b32 v11, -1, v11
	s_nop 0
	v_lshlrev_b32_e32 v11, 2, v11
	v_xor_b32_e32 v11, 64, v11
	ds_bpermute_b32 v11, v11, v10
	s_waitcnt lgkmcnt(0)
	v_add_f32_e32 v10, v10, v11
	v_mbcnt_lo_u32_b32 v11, -1, 0
	v_mbcnt_hi_u32_b32 v11, -1, v11
	v_mbcnt_lo_u32_b32 v15, -1, 0
	v_mbcnt_hi_u32_b32 v15, -1, v15
	v_mbcnt_lo_u32_b32 v17, -1, 0
	v_mbcnt_hi_u32_b32 v17, -1, v17
	v_mbcnt_lo_u32_b32 v21, -1, 0
	v_mbcnt_hi_u32_b32 v21, -1, v21
	v_mbcnt_lo_u32_b32 v23, -1, 0
	v_mbcnt_hi_u32_b32 v23, -1, v23
	v_mbcnt_lo_u32_b32 v26, -1, 0
	v_mbcnt_hi_u32_b32 v26, -1, v26
	v_mbcnt_lo_u32_b32 v27, -1, 0
	v_mbcnt_hi_u32_b32 v27, -1, v27
	s_nop 0
	v_lshlrev_b32_e32 v15, 2, v15
	v_lshlrev_b32_e32 v17, 2, v17
	v_xor_b32_e32 v17, 8, v17
	v_lshlrev_b32_e32 v23, 2, v23
	v_pk_fma_f32 v[0:1], v[0:1], v[16:17], v[12:13] op_sel_hi:[1,0,1]
	v_lshlrev_b32_e32 v21, 2, v21
	v_xor_b32_e32 v23, 32, v23
	v_pk_fma_f32 v[0:1], v[2:3], v[24:25], v[0:1] op_sel_hi:[1,0,1]
	v_xor_b32_e32 v21, 16, v21
	v_mbcnt_lo_u32_b32 v28, -1, 0
	v_mbcnt_hi_u32_b32 v28, -1, v28
	v_pk_fma_f32 v[0:1], v[4:5], v[22:23], v[0:1] op_sel_hi:[1,0,1]
	v_xor_b32_e32 v15, 4, v15
	v_lshlrev_b32_e32 v28, 2, v28
	v_pk_fma_f32 v[0:1], v[6:7], v[20:21], v[0:1] op_sel_hi:[1,0,1]
	v_xor_b32_e32 v28, 4, v28
	v_pk_fma_f32 v[0:1], v[8:9], v[14:15], v[0:1] op_sel_hi:[1,0,1]
	v_mbcnt_lo_u32_b32 v41, -1, 0
	v_mbcnt_hi_u32_b32 v41, -1, v41
	v_lshlrev_b32_e32 v41, 2, v41
	v_xor_b32_e32 v42, 4, v41
	ds_bpermute_b32 v2, v42, v0
	ds_bpermute_b32 v3, v42, v1
	ds_bpermute_b32 v43, v42, v39
	ds_bpermute_b32 v44, v42, v37
	ds_bpermute_b32 v45, v42, v35
	ds_bpermute_b32 v46, v42, v33
	ds_bpermute_b32 v47, v42, v31
	ds_bpermute_b32 v48, v42, v29
	s_waitcnt lgkmcnt(0)
	v_pk_add_f32 v[0:1], v[0:1], v[2:3]
	v_add_f32_e32 v39, v39, v43
	v_add_f32_e32 v37, v37, v44
	v_add_f32_e32 v35, v35, v45
	v_add_f32_e32 v33, v33, v46
	v_add_f32_e32 v31, v31, v47
	v_add_f32_e32 v29, v29, v48
	v_xor_b32_e32 v42, 8, v41
	ds_bpermute_b32 v2, v42, v0
	ds_bpermute_b32 v3, v42, v1
	ds_bpermute_b32 v43, v42, v39
	ds_bpermute_b32 v44, v42, v37
	ds_bpermute_b32 v45, v42, v35
	ds_bpermute_b32 v46, v42, v33
	ds_bpermute_b32 v47, v42, v31
	ds_bpermute_b32 v48, v42, v29
	s_waitcnt lgkmcnt(0)
	v_pk_add_f32 v[0:1], v[0:1], v[2:3]
	v_add_f32_e32 v39, v39, v43
	v_add_f32_e32 v37, v37, v44
	v_add_f32_e32 v35, v35, v45
	v_add_f32_e32 v33, v33, v46
	v_add_f32_e32 v31, v31, v47
	v_add_f32_e32 v29, v29, v48
	v_xor_b32_e32 v42, 16, v41
	ds_bpermute_b32 v2, v42, v0
	ds_bpermute_b32 v3, v42, v1
	ds_bpermute_b32 v43, v42, v39
	ds_bpermute_b32 v44, v42, v37
	ds_bpermute_b32 v45, v42, v35
	ds_bpermute_b32 v46, v42, v33
	ds_bpermute_b32 v47, v42, v31
	ds_bpermute_b32 v48, v42, v29
	s_waitcnt lgkmcnt(0)
	v_pk_add_f32 v[0:1], v[0:1], v[2:3]
	v_add_f32_e32 v39, v39, v43
	v_add_f32_e32 v37, v37, v44
	v_add_f32_e32 v35, v35, v45
	v_add_f32_e32 v33, v33, v46
	v_add_f32_e32 v31, v31, v47
	v_add_f32_e32 v29, v29, v48
	v_xor_b32_e32 v42, 32, v41
	ds_bpermute_b32 v2, v42, v0
	ds_bpermute_b32 v3, v42, v1
	ds_bpermute_b32 v43, v42, v39
	ds_bpermute_b32 v44, v42, v37
	ds_bpermute_b32 v45, v42, v35
	ds_bpermute_b32 v46, v42, v33
	ds_bpermute_b32 v47, v42, v31
	ds_bpermute_b32 v48, v42, v29
	s_waitcnt lgkmcnt(0)
	v_pk_add_f32 v[0:1], v[0:1], v[2:3]
	v_add_f32_e32 v39, v39, v43
	v_add_f32_e32 v37, v37, v44
	v_add_f32_e32 v35, v35, v45
	v_add_f32_e32 v33, v33, v46
	v_add_f32_e32 v31, v31, v47
	v_add_f32_e32 v29, v29, v48
	v_xor_b32_e32 v42, 64, v41
	ds_bpermute_b32 v2, v42, v0
	ds_bpermute_b32 v3, v42, v1
	ds_bpermute_b32 v43, v42, v39
	ds_bpermute_b32 v44, v42, v37
	ds_bpermute_b32 v45, v42, v35
	ds_bpermute_b32 v46, v42, v33
	ds_bpermute_b32 v47, v42, v31
	ds_bpermute_b32 v48, v42, v29
	s_waitcnt lgkmcnt(0)
	v_pk_add_f32 v[0:1], v[0:1], v[2:3]
	v_add_f32_e32 v39, v39, v43
	v_add_f32_e32 v37, v37, v44
	v_add_f32_e32 v35, v35, v45
	v_add_f32_e32 v33, v33, v46
	v_add_f32_e32 v31, v31, v47
	v_add_f32_e32 v29, v29, v48
	v_xor_b32_e32 v42, 0x80, v41
	ds_bpermute_b32 v2, v42, v0
	ds_bpermute_b32 v3, v42, v1
	ds_bpermute_b32 v11, v42, v10
	ds_bpermute_b32 v6, v42, v39
	ds_bpermute_b32 v8, v42, v37
	ds_bpermute_b32 v12, v42, v35
	ds_bpermute_b32 v14, v42, v33
	ds_bpermute_b32 v16, v42, v31
	ds_bpermute_b32 v20, v42, v29
	v_mov_b32_e32 v5, v39
	v_mov_b32_e32 v7, v37
	v_mov_b32_e32 v9, v35
	v_mov_b32_e32 v13, v33
	v_mov_b32_e32 v15, v31
	v_mov_b32_e32 v17, v29
	s_waitcnt lgkmcnt(0)
	s_and_saveexec_b64 s[0:1], s[36:37]
	s_cbranch_execz .LBB0_1621
	v_add_f32_e32 v4, v10, v11
	v_fmamk_f32 v4, v4, 0x3a000000, v253
	s_mov_b32 s13, 0xf800000
	v_cmp_gt_f32_e32 vcc, s13, v4
	v_mul_f32_e32 v10, 0x4f800000, v4
	v_add_f32_e32 v5, v5, v6
	v_cndmask_b32_e32 v4, v4, v10, vcc
	v_sqrt_f32_e32 v10, v4
	v_pk_add_f32 v[0:1], v[0:1], v[2:3]
	v_add_f32_e32 v7, v7, v8
	v_add_f32_e32 v9, v9, v12
	v_add_u32_e32 v11, -1, v10
	v_fma_f32 v21, -v11, v10, v4
	v_cmp_ge_f32_e64 s[38:39], 0, v21
	v_add_u32_e32 v21, 1, v10
	v_add_f32_e32 v13, v13, v14
	v_cndmask_b32_e64 v11, v10, v11, s[38:39]
	v_fma_f32 v10, -v21, v10, v4
	v_cmp_lt_f32_e64 s[38:39], 0, v10
	s_nop 1
	v_cndmask_b32_e64 v10, v11, v21, s[38:39]
	v_mul_f32_e32 v11, 0x37800000, v10
	v_cndmask_b32_e32 v10, v10, v11, vcc
	v_mov_b32_e32 v11, 0x260
	v_cmp_class_f32_e32 vcc, v4, v11
	s_nop 1
	v_cndmask_b32_e32 v4, v10, v4, vcc
	v_div_scale_f32 v10, s[18:19], v4, v4, 1.0
	v_rcp_f32_e32 v11, v10
	s_nop 0
	v_fma_f32 v21, -v10, v11, 1.0
	v_fmac_f32_e32 v11, v21, v11
	v_div_scale_f32 v21, vcc, 1.0, v4, 1.0
	v_mul_f32_e32 v22, v21, v11
	v_fma_f32 v23, -v10, v22, v21
	v_fmac_f32_e32 v22, v23, v11
	v_fma_f32 v10, -v10, v22, v21
	v_div_fmas_f32 v10, v10, v11, v22
	v_div_fixup_f32 v4, v10, v4, 1.0
	v_mul_f32_e32 v5, v4, v5
	v_pk_mul_f32 v[0:1], v[4:5], v[0:1] op_sel_hi:[0,1]
	v_cmp_gt_f32_e32 vcc, v1, v0
	v_mul_f32_e32 v7, v4, v7
	v_mul_f32_e32 v9, v4, v9
	v_cndmask_b32_e32 v2, v0, v1, vcc
	v_cmp_gt_f32_e64 s[38:39], v5, v2
	v_mul_f32_e32 v13, v4, v13
	v_cndmask_b32_e64 v3, 0, 1, vcc
	v_cndmask_b32_e64 v2, v2, v5, s[38:39]
	v_cmp_gt_f32_e64 s[40:41], v7, v2
	v_add_f32_e32 v11, v15, v16
	v_cndmask_b32_e64 v3, v3, 2, s[38:39]
	v_cndmask_b32_e64 v2, v2, v7, s[40:41]
	v_cmp_gt_f32_e64 s[42:43], v9, v2
	v_mul_f32_e32 v11, v4, v11
	v_cndmask_b32_e64 v3, v3, 3, s[40:41]
	v_cndmask_b32_e64 v2, v2, v9, s[42:43]
	v_cmp_gt_f32_e64 s[44:45], v13, v2
	s_waitcnt lgkmcnt(0)
	v_add_f32_e32 v10, v17, v20
	v_cndmask_b32_e64 v3, v3, 4, s[42:43]
	v_cndmask_b32_e64 v2, v2, v13, s[44:45]
	v_cmp_gt_f32_e64 s[46:47], v11, v2
	v_mul_f32_e32 v10, v4, v10
	v_cndmask_b32_e64 v3, v3, 5, s[44:45]
	v_cndmask_b32_e64 v2, v2, v11, s[46:47]
	v_cmp_ngt_f32_e64 s[48:49], v10, v2
	v_cndmask_b32_e64 v3, v3, 6, s[46:47]
	s_and_b64 s[18:19], s[48:49], s[46:47]
	v_cndmask_b32_e64 v176, 7, v3, s[48:49]
	v_cmp_ne_u32_e64 s[46:47], 0, v176
	v_cmp_lt_f32_e64 s[50:51], s11, v0
	s_and_b64 s[46:47], s[46:47], s[50:51]
	v_mov_b32_e32 v3, 0xff61b1e6
	v_cndmask_b32_e64 v0, v3, v0, s[46:47]
	v_cmp_ne_u32_e64 s[44:45], 1, v176
	v_cmp_gt_f32_e64 s[46:47], v1, v0
	s_and_b64 s[44:45], s[44:45], s[46:47]
	v_cndmask_b32_e64 v0, v0, v1, s[44:45]
	v_cmp_ne_u32_e64 s[42:43], 2, v176
	v_cmp_gt_f32_e64 s[46:47], v5, v0
	s_and_b64 s[42:43], s[42:43], s[46:47]
	v_cndmask_b32_e64 v0, v0, v5, s[42:43]
	v_cmp_ne_u32_e64 s[40:41], 3, v176
	v_cmp_gt_f32_e64 s[46:47], v7, v0
	s_and_b64 s[40:41], s[40:41], s[46:47]
	v_cndmask_b32_e64 v0, v0, v7, s[40:41]
	v_cmp_ne_u32_e64 s[38:39], 4, v176
	v_cmp_gt_f32_e64 s[46:47], v9, v0
	s_and_b64 s[38:39], s[38:39], s[46:47]
	v_cndmask_b32_e64 v0, v0, v9, s[38:39]
	v_cmp_ne_u32_e32 vcc, 5, v176
	v_cmp_gt_f32_e64 s[46:47], v13, v0
	s_and_b64 vcc, vcc, s[46:47]
	v_cndmask_b32_e32 v0, v0, v13, vcc
	v_cmp_ngt_f32_e64 s[46:47], v11, v0
	s_or_b64 s[46:47], s[18:19], s[46:47]
	v_cndmask_b32_e64 v2, v10, v2, s[48:49]
	v_cndmask_b32_e64 v1, v11, v0, s[46:47]
	v_cmp_gt_f32_e64 s[50:51], v10, v1
	s_and_b64 s[50:51], s[48:49], s[50:51]
	v_cndmask_b32_e64 v0, 0, 1, s[44:45]
	v_cndmask_b32_e64 v1, v1, v10, s[50:51]
	v_sub_f32_e32 v1, v2, v1
	v_mul_f32_e32 v1, 0x3fb8aa3b, v1
	v_exp_f32_e32 v1, v1
	v_cndmask_b32_e64 v0, v0, 2, s[42:43]
	v_cndmask_b32_e64 v0, v0, 3, s[40:41]
	v_cndmask_b32_e64 v0, v0, 4, s[38:39]
	v_add_f32_e32 v1, 1.0, v1
	v_div_scale_f32 v2, s[18:19], v1, v1, 1.0
	v_rcp_f32_e32 v3, v2
	v_cndmask_b32_e64 v0, v0, 5, vcc
	s_add_u32 s18, s52, s8
	s_addc_u32 s19, s53, s9
	v_fma_f32 v5, -v2, v3, 1.0
	v_fmac_f32_e32 v3, v5, v3
	v_div_scale_f32 v5, vcc, 1.0, v1, 1.0
	v_mul_f32_e32 v6, v5, v3
	v_fma_f32 v7, -v2, v6, v5
	v_fmac_f32_e32 v6, v7, v3
	v_fma_f32 v2, -v2, v6, v5
	v_div_fmas_f32 v2, v2, v3, v6
	v_div_fixup_f32 v5, v2, v1, 1.0
	global_store_dword v177, v4, s[18:19]
	v_mul_u32_u24_e32 v2, 0x2100, v176
	v_mov_b32_e32 v3, v177
	v_lshl_add_u64 v[2:3], v[2:3], 0, s[52:53]
	global_atomic_add v1, v[2:3], v231, off offset:384 sc0
	v_cndmask_b32_e64 v0, 6, v0, s[46:47]
	v_cndmask_b32_e64 v0, v0, 7, s[50:51]
	v_mul_u32_u24_e32 v6, 0x2100, v0
	v_mov_b32_e32 v7, v177
	v_lshl_add_u64 v[6:7], v[6:7], 0, s[52:53]
	global_atomic_add v76, v[6:7], v231, off offset:384 sc0
	v_mov_b32_e32 v11, s56
	s_ashr_i32 s67, s66, 31
	s_lshl_b64 s[18:19], s[66:67], 2
	s_add_u32 s20, s2, s18
	s_addc_u32 s21, s3, s19
	s_add_i32 s22, s66, 1
	s_ashr_i32 s23, s22, 31
	s_add_u32 s18, s4, s18
	v_sub_f32_e32 v10, 1.0, v5
	s_addc_u32 s19, s5, s19
	s_waitcnt vmcnt(1)
	v_lshl_add_u32 v176, v176, 14, v1
	v_lshlrev_b64 v[2:3], 2, v[176:177]
	v_lshl_add_u64 v[6:7], s[68:69], 0, v[2:3]
	v_mov_b32_e32 v1, v177
	global_store_dword v[6:7], v11, off
	v_lshl_add_u64 v[2:3], s[70:71], 0, v[2:3]
	global_store_dword v[2:3], v4, off
	s_waitcnt vmcnt(2)
	v_lshl_add_u32 v0, v0, 14, v76
	v_mov_b32_e32 v1, v177
	v_lshlrev_b64 v[6:7], 2, v[0:1]
	v_lshl_add_u64 v[2:3], s[70:71], 0, v[6:7]
	global_store_dword v[2:3], v4, off
	global_store_dword v177, v10, s[18:19]
	s_lshl_b64 s[18:19], s[22:23], 2
	s_add_u32 s18, s4, s18
	v_lshl_add_u64 v[8:9], s[68:69], 0, v[6:7]
	v_mov_b32_e32 v2, v176
	v_mov_b32_e32 v3, v0
	s_addc_u32 s19, s5, s19
	global_store_dword v[8:9], v11, off
	global_store_dwordx2 v177, v[2:3], s[20:21]
	global_store_dword v177, v5, s[18:19]
	s_branch .LBB0_1621
